# P4 EpiResidNorm epilogue: all 16 x-loads per half issued up front into spare VGPRs with counted vmcnt, s_nop 1 after each store for the store-data hazard
# baseline (speedup 1.0000x reference)
.LBB0_457:
	s_lshl_b32 s36, s36, 8
	v_add_u32_e32 v152, s36, v155
	v_lshl_or_b32 v150, s37, 8, v157
	v_ashrrev_i32_e32 v153, 31, v152
	v_ashrrev_i32_e32 v151, 31, v150
	v_lshlrev_b64 v[162:163], 12, v[152:153]
	v_lshl_add_u64 v[170:171], v[162:163], 0, v[150:151]
	v_lshl_add_u64 v[172:173], v[170:171], 2, s[0:1]
	s_mov_b32 s98, 0x40000
	s_mov_b32 s99, 0
	v_mov_b64_e32 v[252:253], v[172:173]
	global_load_dwordx4 v[178:181], v[252:253], off
	global_load_dwordx4 v[182:185], v[252:253], off offset:16
	global_load_dwordx4 v[186:189], v[252:253], off offset:512
	global_load_dwordx4 v[190:193], v[252:253], off offset:528
	v_lshl_add_u64 v[252:253], v[252:253], 0, s[98:99]
	global_load_dwordx4 v[194:197], v[252:253], off
	global_load_dwordx4 v[198:201], v[252:253], off offset:16
	global_load_dwordx4 v[202:205], v[252:253], off offset:512
	global_load_dwordx4 v[206:209], v[252:253], off offset:528
	v_lshl_add_u64 v[252:253], v[252:253], 0, s[98:99]
	global_load_dwordx4 v[210:213], v[252:253], off
	global_load_dwordx4 v[214:217], v[252:253], off offset:16
	global_load_dwordx4 v[218:221], v[252:253], off offset:512
	global_load_dwordx4 v[222:225], v[252:253], off offset:528
	v_lshl_add_u64 v[252:253], v[252:253], 0, s[98:99]
	global_load_dwordx4 v[236:239], v[252:253], off
	global_load_dwordx4 v[240:243], v[252:253], off offset:16
	global_load_dwordx4 v[244:247], v[252:253], off offset:528
	global_load_dwordx4 v[248:251], v[252:253], off offset:512
	v_lshl_add_u64 v[170:171], v[170:171], 1, s[10:11]
	v_xor_b32_e32 v149, 32, v161
	s_nop 0
	s_waitcnt vmcnt(15)
	v_pk_add_f32 v[128:129], v[128:129], v[180:181]
	v_pk_add_f32 v[126:127], v[126:127], v[178:179]
	s_waitcnt vmcnt(14)
	v_pk_add_f32 v[124:125], v[124:125], v[184:185]
	v_pk_add_f32 v[122:123], v[122:123], v[182:183]
	v_cvt_pk_bf16_f32 v162, v126, v127
	v_cvt_pk_bf16_f32 v163, v128, v129
	v_mul_f32_e32 v127, v127, v127
	v_cvt_pk_bf16_f32 v164, v122, v123
	v_cvt_pk_bf16_f32 v165, v124, v125
	global_store_dwordx4 v[170:171], v[162:165], off
	s_nop 1
	s_nop 0
	v_or_b32_e32 v172, 16, v152
	v_ashrrev_i32_e32 v173, 31, v172
	v_lshlrev_b64 v[172:173], 12, v[172:173]
	v_lshl_add_u64 v[172:173], v[172:173], 0, v[150:151]
	v_lshl_add_u64 v[174:175], v[172:173], 2, s[0:1]
	v_mul_f32_e32 v129, v129, v129
	v_mul_f32_e32 v123, v123, v123
	v_mul_f32_e32 v125, v125, v125
	v_fmac_f32_e32 v127, v126, v126
	v_fmac_f32_e32 v129, v128, v128
	v_fmac_f32_e32 v123, v122, v122
	v_fmac_f32_e32 v125, v124, v124
	v_add_f32_e32 v126, v127, v129
	v_add_f32_e32 v127, v123, v125
	s_nop 0
	s_waitcnt vmcnt(14)
	v_pk_add_f32 v[120:121], v[120:121], v[188:189]
	v_pk_add_f32 v[118:119], v[118:119], v[186:187]
	s_nop 0
	s_waitcnt vmcnt(13)
	v_pk_add_f32 v[116:117], v[116:117], v[192:193]
	v_pk_add_f32 v[114:115], v[114:115], v[190:191]
	v_cvt_pk_bf16_f32 v162, v118, v119
	v_cvt_pk_bf16_f32 v163, v120, v121
	s_nop 0
	v_cvt_pk_bf16_f32 v164, v114, v115
	v_cvt_pk_bf16_f32 v165, v116, v117
	global_store_dwordx4 v[170:171], v[162:165], off offset:256
	s_nop 1
	s_nop 0
	v_lshl_add_u64 v[170:171], v[172:173], 1, s[10:11]
	v_or_b32_e32 v172, 32, v152
	v_ashrrev_i32_e32 v173, 31, v172
	v_lshlrev_b64 v[172:173], 12, v[172:173]
	v_lshl_add_u64 v[172:173], v[172:173], 0, v[150:151]
	s_nop 0
	s_waitcnt vmcnt(13)
	v_pk_add_f32 v[112:113], v[112:113], v[196:197]
	v_pk_add_f32 v[110:111], v[110:111], v[194:195]
	s_nop 0
	s_waitcnt vmcnt(12)
	v_pk_add_f32 v[108:109], v[108:109], v[200:201]
	v_pk_add_f32 v[106:107], v[106:107], v[198:199]
	v_cvt_pk_bf16_f32 v162, v110, v111
	v_cvt_pk_bf16_f32 v163, v112, v113
	s_nop 0
	v_cvt_pk_bf16_f32 v164, v106, v107
	v_cvt_pk_bf16_f32 v165, v108, v109
	global_store_dwordx4 v[170:171], v[162:165], off
	s_nop 1
	s_nop 0
	v_lshl_add_u64 v[174:175], v[172:173], 2, s[0:1]
	v_mul_f32_e32 v107, v107, v107
	v_mul_f32_e32 v109, v109, v109
	v_fmac_f32_e32 v107, v106, v106
	v_fmac_f32_e32 v109, v108, v108
	s_nop 0
	s_waitcnt vmcnt(12)
	v_pk_add_f32 v[164:165], v[104:105], v[204:205]
	v_pk_add_f32 v[162:163], v[102:103], v[202:203]
	s_nop 0
	s_waitcnt vmcnt(11)
	v_pk_add_f32 v[168:169], v[100:101], v[208:209]
	v_pk_add_f32 v[166:167], v[98:99], v[206:207]
	v_cvt_pk_bf16_f32 v98, v162, v163
	v_cvt_pk_bf16_f32 v99, v164, v165
	v_mul_f32_e32 v106, v165, v165
	v_cvt_pk_bf16_f32 v100, v166, v167
	v_cvt_pk_bf16_f32 v101, v168, v169
	global_store_dwordx4 v[170:171], v[98:101], off offset:256
	s_nop 1
	s_nop 0
	v_lshl_add_u64 v[170:171], v[172:173], 1, s[10:11]
	v_or_b32_e32 v172, 48, v152
	v_ashrrev_i32_e32 v173, 31, v172
	v_lshlrev_b64 v[172:173], 12, v[172:173]
	v_lshl_add_u64 v[172:173], v[172:173], 0, v[150:151]
	v_mul_f32_e32 v108, v169, v169
	v_fmac_f32_e32 v106, v164, v164
	v_fmac_f32_e32 v108, v168, v168
	s_nop 0
	s_waitcnt vmcnt(11)
	v_pk_add_f32 v[100:101], v[96:97], v[212:213]
	v_pk_add_f32 v[98:99], v[94:95], v[210:211]
	s_nop 0
	s_waitcnt vmcnt(10)
	v_pk_add_f32 v[104:105], v[92:93], v[216:217]
	v_pk_add_f32 v[102:103], v[90:91], v[214:215]
	v_cvt_pk_bf16_f32 v90, v98, v99
	v_cvt_pk_bf16_f32 v91, v100, v101
	s_nop 0
	v_cvt_pk_bf16_f32 v92, v102, v103
	v_cvt_pk_bf16_f32 v93, v104, v105
	global_store_dwordx4 v[170:171], v[90:93], off
	s_nop 1
	s_nop 0
	v_lshl_add_u64 v[174:175], v[172:173], 2, s[0:1]
	s_nop 0
	s_waitcnt vmcnt(10)
	v_pk_add_f32 v[92:93], v[88:89], v[220:221]
	v_pk_add_f32 v[176:177], v[86:87], v[218:219]
	s_nop 0
	s_waitcnt vmcnt(9)
	v_pk_add_f32 v[96:97], v[84:85], v[224:225]
	v_pk_add_f32 v[94:95], v[82:83], v[222:223]
	v_cvt_pk_bf16_f32 v82, v176, v177
	v_cvt_pk_bf16_f32 v83, v92, v93
	v_mul_f32_e32 v93, v93, v93
	v_cvt_pk_bf16_f32 v84, v94, v95
	v_cvt_pk_bf16_f32 v85, v96, v97
	global_store_dwordx4 v[170:171], v[82:85], off offset:256
	s_nop 1
	s_nop 0
	v_lshl_add_u64 v[170:171], v[172:173], 1, s[10:11]
	v_and_b32_e32 v83, 64, v161
	v_xor_b32_e32 v82, 16, v161
	v_add_u32_e32 v83, 64, v83
	v_cmp_lt_i32_e32 vcc, v82, v83
	v_mul_f32_e32 v95, v95, v95
	v_mul_f32_e32 v97, v97, v97
	v_cndmask_b32_e32 v82, v161, v82, vcc
	v_cmp_lt_i32_e32 vcc, v149, v83
	v_mul_f32_e32 v83, v99, v99
	v_mul_f32_e32 v99, v101, v101
	v_mul_f32_e32 v101, v103, v103
	v_mul_f32_e32 v103, v105, v105
	v_fmac_f32_e32 v83, v98, v98
	v_fmac_f32_e32 v99, v100, v100
	v_fmac_f32_e32 v101, v102, v102
	v_fmac_f32_e32 v103, v104, v104
	v_add_f32_e32 v83, v83, v99
	v_add_f32_e32 v98, v101, v103
	v_add_f32_e32 v83, v83, v98
	v_mul_f32_e32 v98, v177, v177
	v_fmac_f32_e32 v98, v176, v176
	v_fmac_f32_e32 v93, v92, v92
	v_fmac_f32_e32 v95, v94, v94
	v_fmac_f32_e32 v97, v96, v96
	v_add_f32_e32 v92, v98, v93
	v_add_f32_e32 v93, v95, v97
	v_add_f32_e32 v92, v92, v93
	v_lshlrev_b32_e32 v82, 2, v82
	v_add_f32_e32 v83, v83, v92
	ds_bpermute_b32 v92, v82, v83
	s_nop 0
	s_waitcnt vmcnt(9)
	v_pk_add_f32 v[122:123], v[80:81], v[238:239]
	v_pk_add_f32 v[124:125], v[78:79], v[236:237]
	s_nop 0
	s_waitcnt vmcnt(8)
	v_pk_add_f32 v[90:91], v[76:77], v[242:243]
	v_pk_add_f32 v[88:89], v[74:75], v[240:241]
	v_cvt_pk_bf16_f32 v74, v124, v125
	v_cvt_pk_bf16_f32 v75, v122, v123
	v_mul_f32_e32 v93, v125, v125
	v_cvt_pk_bf16_f32 v76, v88, v89
	v_cvt_pk_bf16_f32 v77, v90, v91
	global_store_dwordx4 v[170:171], v[74:77], off
	s_nop 1
	v_mul_f32_e32 v75, v119, v119
	v_mul_f32_e32 v76, v121, v121
	v_mul_f32_e32 v77, v115, v115
	v_mul_f32_e32 v115, v117, v117
	v_fmac_f32_e32 v75, v118, v118
	v_fmac_f32_e32 v76, v120, v120
	v_fmac_f32_e32 v77, v114, v114
	v_fmac_f32_e32 v115, v116, v116
	v_add_f32_e32 v75, v75, v76
	v_add_f32_e32 v76, v77, v115
	v_add_f32_e32 v74, v126, v127
	v_add_f32_e32 v75, v75, v76
	v_add_f32_e32 v75, v74, v75
	v_mul_f32_e32 v74, v111, v111
	v_mul_f32_e32 v77, v113, v113
	v_fmac_f32_e32 v74, v110, v110
	v_fmac_f32_e32 v77, v112, v112
	v_add_f32_e32 v74, v74, v77
	v_add_f32_e32 v77, v107, v109
	v_add_f32_e32 v74, v74, v77
	v_mul_f32_e32 v77, v163, v163
	v_mul_f32_e32 v107, v167, v167
	v_mul_f32_e32 v94, v123, v123
	v_mul_f32_e32 v89, v89, v89
	v_mul_f32_e32 v91, v91, v91
	v_fmac_f32_e32 v77, v162, v162
	v_fmac_f32_e32 v107, v166, v166
	v_fmac_f32_e32 v93, v124, v124
	v_fmac_f32_e32 v94, v122, v122
	v_fmac_f32_e32 v89, v88, v88
	v_fmac_f32_e32 v91, v90, v90
	v_add_f32_e32 v77, v77, v106
	v_add_f32_e32 v106, v107, v108
	v_add_f32_e32 v88, v93, v94
	v_add_f32_e32 v89, v89, v91
	v_add_f32_e32 v77, v77, v106
	v_add_f32_e32 v88, v88, v89
	v_add_f32_e32 v106, v74, v77
	ds_bpermute_b32 v76, v82, v75
	ds_bpermute_b32 v107, v82, v106
	v_cndmask_b32_e32 v74, v161, v149, vcc
	v_lshlrev_b32_e32 v74, 2, v74
	v_cmp_lt_i32_e32 vcc, 0, v154
	s_waitcnt lgkmcnt(1)
	v_add_f32_e32 v76, v75, v76
	s_waitcnt lgkmcnt(0)
	v_add_f32_e32 v75, v106, v107
	ds_bpermute_b32 v77, v74, v76
	s_nop 0
	s_waitcnt vmcnt(7)
	v_pk_add_f32 v[72:73], v[72:73], v[250:251]
	v_pk_add_f32 v[70:71], v[70:71], v[248:249]
	v_pk_add_f32 v[84:85], v[68:69], v[246:247]
	v_pk_add_f32 v[80:81], v[66:67], v[244:245]
	v_mul_f32_e32 v66, v71, v71
	v_mul_f32_e32 v67, v73, v73
	v_mul_f32_e32 v68, v81, v81
	v_mul_f32_e32 v69, v85, v85
	v_fmac_f32_e32 v66, v70, v70
	v_fmac_f32_e32 v67, v72, v72
	v_fmac_f32_e32 v68, v80, v80
	v_fmac_f32_e32 v69, v84, v84
	v_add_f32_e32 v66, v66, v67
	v_add_f32_e32 v67, v68, v69
	v_add_f32_e32 v66, v66, v67
	v_add_f32_e32 v68, v88, v66
	ds_bpermute_b32 v79, v82, v68
	v_add_f32_e32 v67, v83, v92
	v_cvt_pk_bf16_f32 v78, v70, v71
	ds_bpermute_b32 v66, v74, v75
	ds_bpermute_b32 v69, v74, v67
	s_waitcnt lgkmcnt(2)
	v_add_f32_e32 v70, v68, v79
	ds_bpermute_b32 v71, v74, v70
	v_cvt_pk_bf16_f32 v79, v72, v73
	v_cvt_pk_bf16_f32 v80, v80, v81
	v_cvt_pk_bf16_f32 v81, v84, v85
	global_store_dwordx4 v[170:171], v[78:81], off offset:256
	s_nop 1
	s_and_saveexec_b64 s[38:39], vcc
	s_xor_b64 s[38:39], exec, s[38:39]
	s_cbranch_execz .LBB0_463
	v_cmp_ne_u32_e32 vcc, 1, v154
	s_and_saveexec_b64 s[40:41], vcc
	s_xor_b64 s[40:41], exec, s[40:41]
	s_cbranch_execz .LBB0_460
	s_waitcnt lgkmcnt(0)
	v_add_f32_e32 v66, v70, v71
	v_add_f32_e32 v67, v67, v69
	v_cndmask_b32_e64 v68, v66, v67, s[4:5]

.LBB0_463:
	s_andn2_saveexec_b64 s[38:39], s[38:39]
	v_add_f32_e32 v68, v76, v77
	s_or_b64 exec, exec, s[38:39]
	s_lshl_b32 s27, s37, 2
	s_or_b32 s38, s27, s59
	s_ashr_i32 s39, s38, 31
	s_ashr_i32 s37, s36, 31
	s_lshl_b64 s[38:39], s[38:39], 15
	s_add_u32 s27, s57, s38
	s_addc_u32 s29, s58, s39
	s_lshl_b64 s[36:37], s[36:37], 2
	s_add_u32 s27, s27, s36
	s_addc_u32 s29, s29, s37
	s_add_u32 s36, s27, s16
	s_addc_u32 s37, s29, s17
	s_waitcnt lgkmcnt(2)
	v_lshl_add_u64 v[66:67], s[36:37], 0, v[138:139]
	v_mov_b32_e32 v149, v139
	v_lshl_add_u64 v[66:67], v[66:67], 0, v[148:149]
	global_store_dword v[66:67], v68, off
	s_nop 1
	s_waitcnt lgkmcnt(1)
	v_lshlrev_b64 v[68:69], 12, v[152:153]
	v_lshl_add_u64 v[68:69], v[68:69], 0, v[150:151]
	v_lshl_add_u64 v[80:81], v[68:69], 0, s[18:19]
	v_lshl_add_u64 v[84:85], v[80:81], 2, s[0:1]
	s_mov_b32 s98, 0x40000
	s_mov_b32 s99, 0
	v_mov_b64_e32 v[252:253], v[84:85]
	global_load_dwordx4 v[178:181], v[252:253], off
	global_load_dwordx4 v[182:185], v[252:253], off offset:16
	global_load_dwordx4 v[186:189], v[252:253], off offset:512
	global_load_dwordx4 v[190:193], v[252:253], off offset:528
	v_lshl_add_u64 v[252:253], v[252:253], 0, s[98:99]
	global_load_dwordx4 v[194:197], v[252:253], off
	global_load_dwordx4 v[198:201], v[252:253], off offset:16
	global_load_dwordx4 v[202:205], v[252:253], off offset:512
	global_load_dwordx4 v[206:209], v[252:253], off offset:528
	v_lshl_add_u64 v[252:253], v[252:253], 0, s[98:99]
	global_load_dwordx4 v[210:213], v[252:253], off
	global_load_dwordx4 v[214:217], v[252:253], off offset:16
	global_load_dwordx4 v[218:221], v[252:253], off offset:512
	global_load_dwordx4 v[222:225], v[252:253], off offset:528
	v_lshl_add_u64 v[252:253], v[252:253], 0, s[98:99]
	global_load_dwordx4 v[236:239], v[252:253], off
	global_load_dwordx4 v[240:243], v[252:253], off offset:16
	global_load_dwordx4 v[244:247], v[252:253], off offset:528
	global_load_dwordx4 v[248:251], v[252:253], off offset:512
	s_waitcnt lgkmcnt(0)
	v_lshl_add_u64 v[80:81], v[80:81], 1, s[10:11]
	v_cmp_lt_i32_e32 vcc, 0, v154
	s_nop 0
	s_waitcnt vmcnt(15)
	v_pk_add_f32 v[64:65], v[64:65], v[180:181]
	v_pk_add_f32 v[62:63], v[62:63], v[178:179]
	s_nop 0
	s_waitcnt vmcnt(14)
	v_pk_add_f32 v[60:61], v[60:61], v[184:185]
	v_pk_add_f32 v[58:59], v[58:59], v[182:183]
	v_cvt_pk_bf16_f32 v70, v62, v63
	v_cvt_pk_bf16_f32 v71, v64, v65
	v_mul_f32_e32 v63, v63, v63
	v_cvt_pk_bf16_f32 v72, v58, v59
	v_cvt_pk_bf16_f32 v73, v60, v61
	global_store_dwordx4 v[80:81], v[70:73], off
	s_nop 1
	s_nop 0
	v_lshl_add_u64 v[84:85], v[68:69], 0, s[20:21]
	v_lshl_add_u64 v[86:87], v[84:85], 2, s[0:1]
	v_mul_f32_e32 v75, v59, v59
	v_fmac_f32_e32 v75, v58, v58
	v_mul_f32_e32 v65, v65, v65
	v_fmac_f32_e32 v63, v62, v62
	v_fmac_f32_e32 v65, v64, v64
	v_add_f32_e32 v62, v63, v65
	s_nop 0
	s_waitcnt vmcnt(14)
	v_pk_add_f32 v[56:57], v[56:57], v[188:189]
	v_pk_add_f32 v[54:55], v[54:55], v[186:187]
	s_nop 0
	s_waitcnt vmcnt(13)
	v_pk_add_f32 v[52:53], v[52:53], v[192:193]
	v_pk_add_f32 v[50:51], v[50:51], v[190:191]
	v_cvt_pk_bf16_f32 v70, v54, v55
	v_cvt_pk_bf16_f32 v71, v56, v57
	s_nop 0
	v_cvt_pk_bf16_f32 v72, v50, v51
	v_cvt_pk_bf16_f32 v73, v52, v53
	global_store_dwordx4 v[80:81], v[70:73], off offset:256
	s_nop 1
	s_nop 0
	v_lshl_add_u64 v[80:81], v[84:85], 1, s[10:11]
	v_lshl_add_u64 v[84:85], v[68:69], 0, s[22:23]
	v_lshl_add_u64 v[68:69], v[68:69], 0, s[24:25]
	s_nop 0
	s_waitcnt vmcnt(13)
	v_pk_add_f32 v[48:49], v[48:49], v[196:197]
	v_pk_add_f32 v[46:47], v[46:47], v[194:195]
	s_nop 0
	s_waitcnt vmcnt(12)
	v_pk_add_f32 v[44:45], v[44:45], v[200:201]
	v_pk_add_f32 v[42:43], v[42:43], v[198:199]
	v_cvt_pk_bf16_f32 v70, v46, v47
	v_cvt_pk_bf16_f32 v71, v48, v49
	s_nop 0
	v_cvt_pk_bf16_f32 v72, v42, v43
	v_cvt_pk_bf16_f32 v73, v44, v45
	global_store_dwordx4 v[80:81], v[70:73], off
	s_nop 1
	s_nop 0
	v_lshl_add_u64 v[86:87], v[84:85], 2, s[0:1]
	v_mul_f32_e32 v43, v43, v43
	v_mul_f32_e32 v45, v45, v45
	v_fmac_f32_e32 v43, v42, v42
	v_fmac_f32_e32 v45, v44, v44
	s_nop 0
	s_waitcnt vmcnt(12)
	v_pk_add_f32 v[72:73], v[40:41], v[204:205]
	v_pk_add_f32 v[70:71], v[38:39], v[202:203]
	s_nop 0
	s_waitcnt vmcnt(11)
	v_pk_add_f32 v[78:79], v[36:37], v[208:209]
	v_pk_add_f32 v[76:77], v[34:35], v[206:207]
	v_cvt_pk_bf16_f32 v34, v70, v71
	v_cvt_pk_bf16_f32 v35, v72, v73
	v_mul_f32_e32 v42, v73, v73
	v_cvt_pk_bf16_f32 v36, v76, v77
	v_cvt_pk_bf16_f32 v37, v78, v79
	global_store_dwordx4 v[80:81], v[34:37], off offset:256
	s_nop 1
	s_nop 0
	v_lshl_add_u64 v[80:81], v[84:85], 1, s[10:11]
	v_lshl_add_u64 v[84:85], v[68:69], 2, s[0:1]
	v_lshl_add_u64 v[68:69], v[68:69], 1, s[10:11]
	v_mul_f32_e32 v44, v79, v79
	v_fmac_f32_e32 v42, v72, v72
	v_fmac_f32_e32 v44, v78, v78
	s_nop 0
	s_waitcnt vmcnt(11)
	v_pk_add_f32 v[36:37], v[32:33], v[212:213]
	v_pk_add_f32 v[34:35], v[30:31], v[210:211]
	s_nop 0
	s_waitcnt vmcnt(10)
	v_pk_add_f32 v[40:41], v[28:29], v[216:217]
	v_pk_add_f32 v[38:39], v[26:27], v[214:215]
	v_cvt_pk_bf16_f32 v26, v34, v35
	v_cvt_pk_bf16_f32 v27, v36, v37
	s_nop 0
	v_cvt_pk_bf16_f32 v28, v38, v39
	v_cvt_pk_bf16_f32 v29, v40, v41
	global_store_dwordx4 v[80:81], v[26:29], off
	s_nop 1
	s_nop 0
	s_nop 0
	s_waitcnt vmcnt(10)
	v_pk_add_f32 v[28:29], v[24:25], v[220:221]
	v_pk_add_f32 v[26:27], v[22:23], v[218:219]
	s_nop 0
	s_waitcnt vmcnt(9)
	v_pk_add_f32 v[32:33], v[20:21], v[224:225]
	v_pk_add_f32 v[30:31], v[18:19], v[222:223]
	v_cvt_pk_bf16_f32 v18, v26, v27
	v_cvt_pk_bf16_f32 v19, v28, v29
	v_mul_f32_e32 v27, v27, v27
	v_cvt_pk_bf16_f32 v20, v30, v31
	v_cvt_pk_bf16_f32 v21, v32, v33
	global_store_dwordx4 v[80:81], v[18:21], off offset:256
	s_nop 1
	s_nop 0
	v_mul_f32_e32 v80, v61, v61
	v_fmac_f32_e32 v80, v60, v60
	v_mul_f32_e32 v29, v29, v29
	v_mul_f32_e32 v31, v31, v31
	v_mul_f32_e32 v33, v33, v33
	v_fmac_f32_e32 v27, v26, v26
	v_fmac_f32_e32 v29, v28, v28
	v_fmac_f32_e32 v31, v30, v30
	v_fmac_f32_e32 v33, v32, v32
	v_add_f32_e32 v26, v27, v29
	v_add_f32_e32 v27, v31, v33
	v_add_f32_e32 v26, v26, v27
	s_nop 0
	s_waitcnt vmcnt(9)
	v_pk_add_f32 v[58:59], v[16:17], v[238:239]
	v_pk_add_f32 v[60:61], v[14:15], v[236:237]
	s_nop 0
	s_waitcnt vmcnt(8)
	v_pk_add_f32 v[24:25], v[12:13], v[242:243]
	v_pk_add_f32 v[22:23], v[10:11], v[240:241]
	v_cvt_pk_bf16_f32 v10, v60, v61
	v_cvt_pk_bf16_f32 v11, v58, v59
	v_mul_f32_e32 v27, v61, v61
	v_cvt_pk_bf16_f32 v12, v22, v23
	v_cvt_pk_bf16_f32 v13, v24, v25
	global_store_dwordx4 v[68:69], v[10:13], off
	s_nop 1
	v_mul_f32_e32 v11, v55, v55
	v_mul_f32_e32 v12, v57, v57
	v_mul_f32_e32 v13, v51, v51
	v_mul_f32_e32 v51, v53, v53
	v_fmac_f32_e32 v11, v54, v54
	v_fmac_f32_e32 v12, v56, v56
	v_fmac_f32_e32 v13, v50, v50
	v_fmac_f32_e32 v51, v52, v52
	v_add_f32_e32 v11, v11, v12
	v_add_f32_e32 v12, v13, v51
	v_add_f32_e32 v11, v11, v12
	v_mul_f32_e32 v12, v47, v47
	v_mul_f32_e32 v13, v49, v49
	v_fmac_f32_e32 v12, v46, v46
	v_fmac_f32_e32 v13, v48, v48
	v_add_f32_e32 v12, v12, v13
	v_add_f32_e32 v13, v43, v45
	v_add_f32_e32 v12, v12, v13
	v_mul_f32_e32 v13, v71, v71
	v_mul_f32_e32 v43, v77, v77
	v_fmac_f32_e32 v13, v70, v70
	v_fmac_f32_e32 v43, v76, v76
	v_add_f32_e32 v10, v75, v80
	v_add_f32_e32 v13, v13, v42
	v_add_f32_e32 v42, v43, v44
	v_add_f32_e32 v10, v62, v10
	v_add_f32_e32 v13, v13, v42
	v_add_f32_e32 v10, v10, v11
	v_add_f32_e32 v13, v12, v13
	ds_bpermute_b32 v11, v82, v10
	ds_bpermute_b32 v42, v82, v13
	v_mul_f32_e32 v28, v59, v59
	v_mul_f32_e32 v23, v23, v23
	v_mul_f32_e32 v25, v25, v25
	s_waitcnt lgkmcnt(1)
	v_add_f32_e32 v11, v10, v11
	s_waitcnt lgkmcnt(0)
	v_add_f32_e32 v10, v13, v42
	v_mul_f32_e32 v13, v35, v35
	v_mul_f32_e32 v35, v37, v37
	v_mul_f32_e32 v37, v39, v39
	v_mul_f32_e32 v39, v41, v41
	v_fmac_f32_e32 v13, v34, v34
	v_fmac_f32_e32 v35, v36, v36
	v_fmac_f32_e32 v37, v38, v38
	v_fmac_f32_e32 v39, v40, v40
	v_fmac_f32_e32 v27, v60, v60
	v_fmac_f32_e32 v28, v58, v58
	v_fmac_f32_e32 v23, v22, v22
	v_fmac_f32_e32 v25, v24, v24
	v_add_f32_e32 v13, v13, v35
	v_add_f32_e32 v34, v37, v39
	v_add_f32_e32 v22, v27, v28
	v_add_f32_e32 v23, v23, v25
	v_add_f32_e32 v13, v13, v34
	v_add_f32_e32 v22, v22, v23
	v_add_f32_e32 v13, v13, v26
	ds_bpermute_b32 v26, v82, v13
	ds_bpermute_b32 v12, v74, v11
	s_nop 0
	s_waitcnt vmcnt(7)
	v_pk_add_f32 v[8:9], v[8:9], v[250:251]
	v_pk_add_f32 v[6:7], v[6:7], v[248:249]
	v_pk_add_f32 v[18:19], v[4:5], v[246:247]
	v_pk_add_f32 v[16:17], v[2:3], v[244:245]
	v_mul_f32_e32 v2, v7, v7
	v_mul_f32_e32 v3, v9, v9
	v_mul_f32_e32 v4, v17, v17
	v_mul_f32_e32 v5, v19, v19
	v_fmac_f32_e32 v2, v6, v6
	v_fmac_f32_e32 v3, v8, v8
	v_fmac_f32_e32 v4, v16, v16
	v_fmac_f32_e32 v5, v18, v18
	v_add_f32_e32 v2, v2, v3
	v_add_f32_e32 v3, v4, v5
	v_add_f32_e32 v2, v2, v3
	v_add_f32_e32 v2, v22, v2
	ds_bpermute_b32 v15, v82, v2
	s_waitcnt lgkmcnt(2)
	v_add_f32_e32 v4, v13, v26
	v_cvt_pk_bf16_f32 v14, v6, v7
	ds_bpermute_b32 v3, v74, v10
	ds_bpermute_b32 v5, v74, v4
	s_waitcnt lgkmcnt(2)
	v_add_f32_e32 v6, v2, v15
	ds_bpermute_b32 v7, v74, v6
	v_cvt_pk_bf16_f32 v15, v8, v9
	v_cvt_pk_bf16_f32 v16, v16, v17
	v_cvt_pk_bf16_f32 v17, v18, v19
	global_store_dwordx4 v[68:69], v[14:17], off offset:256
	s_nop 1
	s_and_saveexec_b64 s[36:37], vcc
	s_xor_b64 s[36:37], exec, s[36:37]
	s_cbranch_execz .LBB0_471
	v_cmp_ne_u32_e32 vcc, 1, v154
	s_and_saveexec_b64 s[38:39], vcc
	s_xor_b64 s[38:39], exec, s[38:39]
	s_cbranch_execz .LBB0_468
	s_waitcnt lgkmcnt(0)
	v_add_f32_e32 v2, v6, v7
	v_add_f32_e32 v3, v4, v5
	v_cndmask_b32_e64 v2, v2, v3, s[4:5]
